# P9 epilogue with packed f32 math (v_pk_mul_f32 / v_pk_add_f32 on accumulator pairs, same per-element operation order)
# speedup vs baseline: 1.0070x; 1.0070x over previous
.LBB0_901:
	s_add_i32 s98, s29, 1
	s_lshl_b32 s98, s98, 2
	s_add_i32 s98, s98, 0x21160
	v_mov_b32_e32 v240, s98
	ds_read_b32 v240, v240
	s_lshl_b32 s4, s92, 7
	s_and_b32 s4, s4, 0x7f80
	v_add_u32_e32 v2, v218, v183
	v_or_b32_e32 v3, s4, v212
	v_lshl_add_u32 v2, v2, 9, v3
	v_mov_b32_e32 v236, 1.0
	v_mov_b32_e32 v237, 1.0
	v_exp_f32_e32 v12, v162
	v_exp_f32_e32 v13, v163
	v_exp_f32_e32 v14, v164
	v_exp_f32_e32 v15, v165
	v_exp_f32_e32 v16, v158
	v_exp_f32_e32 v17, v159
	v_exp_f32_e32 v18, v160
	v_exp_f32_e32 v19, v161
	v_pk_mul_f32 v[20:21], v[170:171], v[162:163]
	v_pk_mul_f32 v[22:23], v[172:173], v[164:165]
	v_pk_mul_f32 v[24:25], v[166:167], v[158:159]
	v_pk_mul_f32 v[26:27], v[168:169], v[160:161]
	v_pk_add_f32 v[12:13], v[12:13], v[236:237]
	v_pk_add_f32 v[14:15], v[14:15], v[236:237]
	v_pk_add_f32 v[16:17], v[16:17], v[236:237]
	v_pk_add_f32 v[18:19], v[18:19], v[236:237]
	v_rcp_f32_e32 v12, v12
	v_rcp_f32_e32 v13, v13
	v_rcp_f32_e32 v14, v14
	v_rcp_f32_e32 v15, v15
	v_rcp_f32_e32 v16, v16
	v_rcp_f32_e32 v17, v17
	v_rcp_f32_e32 v18, v18
	v_rcp_f32_e32 v19, v19
	v_pk_mul_f32 v[20:21], v[20:21], v[12:13]
	v_pk_mul_f32 v[22:23], v[22:23], v[14:15]
	v_pk_mul_f32 v[24:25], v[24:25], v[16:17]
	v_pk_mul_f32 v[26:27], v[26:27], v[18:19]
	v_med3_f32 v20, v20, s26, v216
	v_med3_f32 v21, v21, s26, v216
	v_med3_f32 v22, v22, s26, v216
	v_med3_f32 v23, v23, s26, v216
	v_med3_f32 v24, v24, s26, v216
	v_med3_f32 v25, v25, s26, v216
	v_med3_f32 v26, v26, s26, v216
	v_med3_f32 v27, v27, s26, v216
	v_cvt_pk_fp8_f32 v4, v20, v21
	v_cvt_pk_fp8_f32 v5, v24, v25
	v_cvt_pk_fp8_f32 v4, v22, v23 op_sel:[0,0,1]
	v_cvt_pk_fp8_f32 v5, v26, v27 op_sel:[0,0,1]
	global_store_dwordx2 v2, v[4:5], s[2:3]
	s_waitcnt lgkmcnt(0)
	v_readfirstlane_b32 s98, v240
	s_max_i32 s98, s98, 0
	s_lshl_b32 s98, s98, 2
	s_add_i32 s98, s98, 0x20200
	v_mov_b32_e32 v241, s98
	ds_read_b32 v242, v241
	ds_read_b32 v243, v241 offset:288
	ds_read_b32 v241, v241 offset:576
	v_exp_f32_e32 v12, v146
	v_exp_f32_e32 v13, v147
	v_exp_f32_e32 v14, v148
	v_exp_f32_e32 v15, v149
	v_exp_f32_e32 v16, v142
	v_exp_f32_e32 v17, v143
	v_exp_f32_e32 v18, v144
	v_exp_f32_e32 v19, v145
	v_pk_mul_f32 v[20:21], v[154:155], v[146:147]
	v_pk_mul_f32 v[22:23], v[156:157], v[148:149]
	v_pk_mul_f32 v[24:25], v[150:151], v[142:143]
	v_pk_mul_f32 v[26:27], v[152:153], v[144:145]
	v_pk_add_f32 v[12:13], v[12:13], v[236:237]
	v_pk_add_f32 v[14:15], v[14:15], v[236:237]
	v_pk_add_f32 v[16:17], v[16:17], v[236:237]
	v_pk_add_f32 v[18:19], v[18:19], v[236:237]
	v_rcp_f32_e32 v12, v12
	v_rcp_f32_e32 v13, v13
	v_rcp_f32_e32 v14, v14
	v_rcp_f32_e32 v15, v15
	v_rcp_f32_e32 v16, v16
	v_rcp_f32_e32 v17, v17
	v_rcp_f32_e32 v18, v18
	v_rcp_f32_e32 v19, v19
	v_pk_mul_f32 v[20:21], v[20:21], v[12:13]
	v_pk_mul_f32 v[22:23], v[22:23], v[14:15]
	v_pk_mul_f32 v[24:25], v[24:25], v[16:17]
	v_pk_mul_f32 v[26:27], v[26:27], v[18:19]
	v_med3_f32 v20, v20, s26, v216
	v_med3_f32 v21, v21, s26, v216
	v_med3_f32 v22, v22, s26, v216
	v_med3_f32 v23, v23, s26, v216
	v_med3_f32 v24, v24, s26, v216
	v_med3_f32 v25, v25, s26, v216
	v_med3_f32 v26, v26, s26, v216
	v_med3_f32 v27, v27, s26, v216
	v_cvt_pk_fp8_f32 v4, v20, v21
	v_cvt_pk_fp8_f32 v5, v24, v25
	v_add_u32_e32 v11, 0x2000, v2
	v_cvt_pk_fp8_f32 v4, v22, v23 op_sel:[0,0,1]
	v_cvt_pk_fp8_f32 v5, v26, v27 op_sel:[0,0,1]
	global_store_dwordx2 v11, v[4:5], s[2:3]
	v_exp_f32_e32 v12, v130
	v_exp_f32_e32 v13, v131
	v_exp_f32_e32 v14, v132
	v_exp_f32_e32 v15, v133
	v_exp_f32_e32 v16, v126
	v_exp_f32_e32 v17, v127
	v_exp_f32_e32 v18, v128
	v_exp_f32_e32 v19, v129
	v_pk_mul_f32 v[20:21], v[138:139], v[130:131]
	v_pk_mul_f32 v[22:23], v[140:141], v[132:133]
	v_pk_mul_f32 v[24:25], v[134:135], v[126:127]
	v_pk_mul_f32 v[26:27], v[136:137], v[128:129]
	v_pk_add_f32 v[12:13], v[12:13], v[236:237]
	v_pk_add_f32 v[14:15], v[14:15], v[236:237]
	v_pk_add_f32 v[16:17], v[16:17], v[236:237]
	v_pk_add_f32 v[18:19], v[18:19], v[236:237]
	v_rcp_f32_e32 v12, v12
	v_rcp_f32_e32 v13, v13
	v_rcp_f32_e32 v14, v14
	v_rcp_f32_e32 v15, v15
	v_rcp_f32_e32 v16, v16
	v_rcp_f32_e32 v17, v17
	v_rcp_f32_e32 v18, v18
	v_rcp_f32_e32 v19, v19
	v_pk_mul_f32 v[20:21], v[20:21], v[12:13]
	v_pk_mul_f32 v[22:23], v[22:23], v[14:15]
	v_pk_mul_f32 v[24:25], v[24:25], v[16:17]
	v_pk_mul_f32 v[26:27], v[26:27], v[18:19]
	v_med3_f32 v20, v20, s26, v216
	v_med3_f32 v21, v21, s26, v216
	v_med3_f32 v22, v22, s26, v216
	v_med3_f32 v23, v23, s26, v216
	v_med3_f32 v24, v24, s26, v216
	v_med3_f32 v25, v25, s26, v216
	v_med3_f32 v26, v26, s26, v216
	v_med3_f32 v27, v27, s26, v216
	v_cvt_pk_fp8_f32 v4, v20, v21
	v_cvt_pk_fp8_f32 v5, v24, v25
	v_add_u32_e32 v11, 0x4000, v2
	v_cvt_pk_fp8_f32 v4, v22, v23 op_sel:[0,0,1]
	v_cvt_pk_fp8_f32 v5, v26, v27 op_sel:[0,0,1]
	global_store_dwordx2 v11, v[4:5], s[2:3]
	v_exp_f32_e32 v12, v110
	v_exp_f32_e32 v13, v111
	v_exp_f32_e32 v14, v112
	v_exp_f32_e32 v15, v113
	v_exp_f32_e32 v16, v106
	v_exp_f32_e32 v17, v107
	v_exp_f32_e32 v18, v108
	v_exp_f32_e32 v19, v109
	v_pk_mul_f32 v[20:21], v[122:123], v[110:111]
	v_pk_mul_f32 v[22:23], v[124:125], v[112:113]
	v_pk_mul_f32 v[24:25], v[102:103], v[106:107]
	v_pk_mul_f32 v[26:27], v[104:105], v[108:109]
	v_pk_add_f32 v[12:13], v[12:13], v[236:237]
	v_pk_add_f32 v[14:15], v[14:15], v[236:237]
	v_pk_add_f32 v[16:17], v[16:17], v[236:237]
	v_pk_add_f32 v[18:19], v[18:19], v[236:237]
	v_rcp_f32_e32 v12, v12
	v_rcp_f32_e32 v13, v13
	v_rcp_f32_e32 v14, v14
	v_rcp_f32_e32 v15, v15
	v_rcp_f32_e32 v16, v16
	v_rcp_f32_e32 v17, v17
	v_rcp_f32_e32 v18, v18
	v_rcp_f32_e32 v19, v19
	v_pk_mul_f32 v[20:21], v[20:21], v[12:13]
	v_pk_mul_f32 v[22:23], v[22:23], v[14:15]
	v_pk_mul_f32 v[24:25], v[24:25], v[16:17]
	v_pk_mul_f32 v[26:27], v[26:27], v[18:19]
	v_med3_f32 v20, v20, s26, v216
	v_med3_f32 v21, v21, s26, v216
	v_med3_f32 v22, v22, s26, v216
	v_med3_f32 v23, v23, s26, v216
	v_med3_f32 v24, v24, s26, v216
	v_med3_f32 v25, v25, s26, v216
	v_med3_f32 v26, v26, s26, v216
	v_med3_f32 v27, v27, s26, v216
	v_cvt_pk_fp8_f32 v4, v20, v21
	v_cvt_pk_fp8_f32 v5, v24, v25
	v_add_u32_e32 v11, 0x6000, v2
	v_cvt_pk_fp8_f32 v4, v22, v23 op_sel:[0,0,1]
	v_cvt_pk_fp8_f32 v5, v26, v27 op_sel:[0,0,1]
	global_store_dwordx2 v11, v[4:5], s[2:3]
	v_exp_f32_e32 v12, v98
	v_exp_f32_e32 v13, v99
	v_exp_f32_e32 v14, v100
	v_exp_f32_e32 v15, v101
	v_exp_f32_e32 v16, v94
	v_exp_f32_e32 v17, v95
	v_exp_f32_e32 v18, v96
	v_exp_f32_e32 v19, v97
	v_pk_mul_f32 v[20:21], v[118:119], v[98:99]
	v_pk_mul_f32 v[22:23], v[120:121], v[100:101]
	v_pk_mul_f32 v[24:25], v[114:115], v[94:95]
	v_pk_mul_f32 v[26:27], v[116:117], v[96:97]
	v_pk_add_f32 v[12:13], v[12:13], v[236:237]
	v_pk_add_f32 v[14:15], v[14:15], v[236:237]
	v_pk_add_f32 v[16:17], v[16:17], v[236:237]
	v_pk_add_f32 v[18:19], v[18:19], v[236:237]
	v_rcp_f32_e32 v12, v12
	v_rcp_f32_e32 v13, v13
	v_rcp_f32_e32 v14, v14
	v_rcp_f32_e32 v15, v15
	v_rcp_f32_e32 v16, v16
	v_rcp_f32_e32 v17, v17
	v_rcp_f32_e32 v18, v18
	v_rcp_f32_e32 v19, v19
	v_pk_mul_f32 v[20:21], v[20:21], v[12:13]
	v_pk_mul_f32 v[22:23], v[22:23], v[14:15]
	v_pk_mul_f32 v[24:25], v[24:25], v[16:17]
	v_pk_mul_f32 v[26:27], v[26:27], v[18:19]
	v_med3_f32 v20, v20, s26, v216
	v_med3_f32 v21, v21, s26, v216
	v_med3_f32 v22, v22, s26, v216
	v_med3_f32 v23, v23, s26, v216
	v_med3_f32 v24, v24, s26, v216
	v_med3_f32 v25, v25, s26, v216
	v_med3_f32 v26, v26, s26, v216
	v_med3_f32 v27, v27, s26, v216
	v_cvt_pk_fp8_f32 v4, v20, v21
	v_cvt_pk_fp8_f32 v5, v24, v25
	v_add_u32_e32 v11, 0x10000, v2
	v_cvt_pk_fp8_f32 v4, v22, v23 op_sel:[0,0,1]
	v_cvt_pk_fp8_f32 v5, v26, v27 op_sel:[0,0,1]
	global_store_dwordx2 v11, v[4:5], s[2:3]
	v_exp_f32_e32 v12, v90
	v_exp_f32_e32 v13, v91
	v_exp_f32_e32 v14, v92
	v_exp_f32_e32 v15, v93
	v_exp_f32_e32 v16, v86
	v_exp_f32_e32 v17, v87
	v_exp_f32_e32 v18, v88
	v_exp_f32_e32 v19, v89
	v_pk_mul_f32 v[20:21], v[62:63], v[90:91]
	v_pk_mul_f32 v[22:23], v[64:65], v[92:93]
	v_pk_mul_f32 v[24:25], v[58:59], v[86:87]
	v_pk_mul_f32 v[26:27], v[60:61], v[88:89]
	v_pk_add_f32 v[12:13], v[12:13], v[236:237]
	v_pk_add_f32 v[14:15], v[14:15], v[236:237]
	v_pk_add_f32 v[16:17], v[16:17], v[236:237]
	v_pk_add_f32 v[18:19], v[18:19], v[236:237]
	v_rcp_f32_e32 v12, v12
	v_rcp_f32_e32 v13, v13
	v_rcp_f32_e32 v14, v14
	v_rcp_f32_e32 v15, v15
	v_rcp_f32_e32 v16, v16
	v_rcp_f32_e32 v17, v17
	v_rcp_f32_e32 v18, v18
	v_rcp_f32_e32 v19, v19
	v_pk_mul_f32 v[20:21], v[20:21], v[12:13]
	v_pk_mul_f32 v[22:23], v[22:23], v[14:15]
	v_pk_mul_f32 v[24:25], v[24:25], v[16:17]
	v_pk_mul_f32 v[26:27], v[26:27], v[18:19]
	v_med3_f32 v20, v20, s26, v216
	v_med3_f32 v21, v21, s26, v216
	v_med3_f32 v22, v22, s26, v216
	v_med3_f32 v23, v23, s26, v216
	v_med3_f32 v24, v24, s26, v216
	v_med3_f32 v25, v25, s26, v216
	v_med3_f32 v26, v26, s26, v216
	v_med3_f32 v27, v27, s26, v216
	v_cvt_pk_fp8_f32 v4, v20, v21
	v_cvt_pk_fp8_f32 v5, v24, v25
	v_add_u32_e32 v11, 0x12000, v2
	v_cvt_pk_fp8_f32 v4, v22, v23 op_sel:[0,0,1]
	v_cvt_pk_fp8_f32 v5, v26, v27 op_sel:[0,0,1]
	global_store_dwordx2 v11, v[4:5], s[2:3]
	v_exp_f32_e32 v12, v82
	v_exp_f32_e32 v13, v83
	v_exp_f32_e32 v14, v84
	v_exp_f32_e32 v15, v85
	v_exp_f32_e32 v16, v78
	v_exp_f32_e32 v17, v79
	v_exp_f32_e32 v18, v80
	v_exp_f32_e32 v19, v81
	v_pk_mul_f32 v[20:21], v[54:55], v[82:83]
	v_pk_mul_f32 v[22:23], v[56:57], v[84:85]
	v_pk_mul_f32 v[24:25], v[50:51], v[78:79]
	v_pk_mul_f32 v[26:27], v[52:53], v[80:81]
	v_pk_add_f32 v[12:13], v[12:13], v[236:237]
	v_pk_add_f32 v[14:15], v[14:15], v[236:237]
	v_pk_add_f32 v[16:17], v[16:17], v[236:237]
	v_pk_add_f32 v[18:19], v[18:19], v[236:237]
	v_rcp_f32_e32 v12, v12
	v_rcp_f32_e32 v13, v13
	v_rcp_f32_e32 v14, v14
	v_rcp_f32_e32 v15, v15
	v_rcp_f32_e32 v16, v16
	v_rcp_f32_e32 v17, v17
	v_rcp_f32_e32 v18, v18
	v_rcp_f32_e32 v19, v19
	v_pk_mul_f32 v[20:21], v[20:21], v[12:13]
	v_pk_mul_f32 v[22:23], v[22:23], v[14:15]
	v_pk_mul_f32 v[24:25], v[24:25], v[16:17]
	v_pk_mul_f32 v[26:27], v[26:27], v[18:19]
	v_med3_f32 v20, v20, s26, v216
	v_med3_f32 v21, v21, s26, v216
	v_med3_f32 v22, v22, s26, v216
	v_med3_f32 v23, v23, s26, v216
	v_med3_f32 v24, v24, s26, v216
	v_med3_f32 v25, v25, s26, v216
	v_med3_f32 v26, v26, s26, v216
	v_med3_f32 v27, v27, s26, v216
	v_cvt_pk_fp8_f32 v4, v20, v21
	v_cvt_pk_fp8_f32 v5, v24, v25
	v_add_u32_e32 v11, 0x14000, v2
	v_cvt_pk_fp8_f32 v4, v22, v23 op_sel:[0,0,1]
	v_cvt_pk_fp8_f32 v5, v26, v27 op_sel:[0,0,1]
	global_store_dwordx2 v11, v[4:5], s[2:3]
	v_exp_f32_e32 v12, v74
	v_exp_f32_e32 v13, v75
	v_exp_f32_e32 v14, v76
	v_exp_f32_e32 v15, v77
	v_exp_f32_e32 v16, v70
	v_exp_f32_e32 v17, v71
	v_exp_f32_e32 v18, v72
	v_exp_f32_e32 v19, v73
	v_pk_mul_f32 v[20:21], v[42:43], v[74:75]
	v_pk_mul_f32 v[22:23], v[44:45], v[76:77]
	v_pk_mul_f32 v[24:25], v[66:67], v[70:71]
	v_pk_mul_f32 v[26:27], v[68:69], v[72:73]
	v_pk_add_f32 v[12:13], v[12:13], v[236:237]
	v_pk_add_f32 v[14:15], v[14:15], v[236:237]
	v_pk_add_f32 v[16:17], v[16:17], v[236:237]
	v_pk_add_f32 v[18:19], v[18:19], v[236:237]
	v_rcp_f32_e32 v12, v12
	v_rcp_f32_e32 v13, v13
	v_rcp_f32_e32 v14, v14
	v_rcp_f32_e32 v15, v15
	v_rcp_f32_e32 v16, v16
	v_rcp_f32_e32 v17, v17
	v_rcp_f32_e32 v18, v18
	v_rcp_f32_e32 v19, v19
	v_pk_mul_f32 v[20:21], v[20:21], v[12:13]
	v_pk_mul_f32 v[22:23], v[22:23], v[14:15]
	v_pk_mul_f32 v[24:25], v[24:25], v[16:17]
	v_pk_mul_f32 v[26:27], v[26:27], v[18:19]
	v_med3_f32 v20, v20, s26, v216
	v_med3_f32 v21, v21, s26, v216
	v_med3_f32 v22, v22, s26, v216
	v_med3_f32 v23, v23, s26, v216
	v_med3_f32 v24, v24, s26, v216
	v_med3_f32 v25, v25, s26, v216
	v_med3_f32 v26, v26, s26, v216
	v_med3_f32 v27, v27, s26, v216
	v_cvt_pk_fp8_f32 v4, v20, v21
	v_cvt_pk_fp8_f32 v5, v24, v25
	v_add_u32_e32 v11, 0x16000, v2
	v_cvt_pk_fp8_f32 v4, v22, v23 op_sel:[0,0,1]
	v_cvt_pk_fp8_f32 v5, v26, v27 op_sel:[0,0,1]
	s_mov_b64 s[4:5], -1
	s_andn2_b64 vcc, exec, s[54:55]
	global_store_dwordx2 v11, v[4:5], s[2:3]
	s_cbranch_vccnz .LBB0_871
	s_andn2_b64 vcc, exec, s[80:81]
	s_cbranch_vccnz .LBB0_870
	s_barrier
	s_branch .LBB0_870
